# p1: loop-invariant dt-bias load hoisted out of the pass loop (its per-pass full wait on the tail of waves 0-3 removed)
# baseline (speedup 1.0000x reference)
; #define INP(i)  ((const float*)(const GAS float*)karg64(8 * (i)))
; #define OUTP()  ((float*)(GAS float*)karg64(232))
; #define F_CTL   ((unsigned*)(WSP() + WS_CTL))
; #define F_MOD   ((float*)(WSP() + WS_MOD))
; #define F_DT    ((float*)(WSP() + WS_DT))
; #define F_INV   ((int*)(WSP() + WS_INV))
; #define F_SAH   ((float*)(WSP() + WS_SAH))
; #define F_HAQ   ((signed char*)(WSP() + WS_HA))
; __device__ __forceinline__ void p1_norm1(const Frame& F, int layer, int probe_rerun) {
;     ...
;     const int gw = F.blk * NWAVES + F.wave, NGW = F.G * NWAVES, lane = F.lane;
;     const int nrows = fin ? NL : NT;
;     const int RW = 2 * ((nrows + 2 * NGW - 1) / (2 * NGW)), rbeg = gw * RW;
;     const float* modl = F_MOD + (size_t)(fin ? 0 : layer) * 17 * 6144;
;     const float* modp = F_MOD + (size_t)(layer > 0 ? layer - 1 : 0) * 17 * 6144;
;     const float* n1w = INP(I_N1W) + (size_t)(fin ? 0 : layer) * D;
;     float* const outp = OUTP(); bf16_t* const xb = F_XB; const bool srcf32 = (layer == 0 && !probe_rerun);
;     const float* const srcl = INP(I_X); const float* const srcc = INP(I_CTX);
;     const int* const invp = F_INV; const bf16_t* const Yp = F_Y; signed char* const HQp = F_HAQ; float* const SAp = F_SAH; float* const DTp = F_DT;
;     const bf16_t* const zrow = (const bf16_t*)(F_CTL + CW_ZERO);
;     const float* const dtbf = INP(I_DTBF) + (fin ? 0 : layer) * 8; const float* const dtbb = INP(I_DTBB) + (fin ? 0 : layer) * 8;
;     const bool comb = (layer > 0 && !probe_rerun);
;     f32x4 nva[4], nvb[4]; int nia = -1, nib = -1;
;     f32x4 W1[4], S0[4], G2[4]; int cur_m = -1;
; #pragma unroll
;     for (int j = 0; j < 4; ++j) { W1[j] = (f32x4){0.f, 0.f, 0.f, 0.f}; S0[j] = W1[j]; G2[j] = W1[j]; }
;     ...
;             const float bias = (c < 8) ? dtbf[c] : dtbb[c - 8]; const int grow = (F.blk * NWAVES + (srow >> 1)) * RW + 2 * pi + (srow & 1);
.LBB0_141:
	s_mov_b32 s62, s66
	s_mov_b32 s63, s31
	s_max_i32 s30, s66, 1
	s_add_i32 s30, s30, -1
	s_lshl_b64 s[36:37], s[62:63], 12
	s_add_u32 s52, s38, 0x44734800
	s_addc_u32 s53, s39, 0
	s_add_u32 s54, s40, 0x8000
	s_mul_i32 s57, s66, 0x66000
	s_mul_hi_u32 s60, s30, 0x66000
	s_mul_i32 s61, s30, 0x66000
	s_addc_u32 s55, s41, 0
	s_lshl_b32 s30, s66, 3
	s_mul_hi_u32 s35, s66, 0x66000
	s_add_u32 s14, s14, s57
	s_addc_u32 s15, s15, s35
	s_add_u32 s14, s14, 0x200000
	s_addc_u32 s15, s15, 0
	s_add_u32 s10, s10, s61
	s_addc_u32 s11, s11, s60
	s_add_u32 s36, s12, s36
	s_addc_u32 s37, s13, s37
	s_add_u32 s12, s16, 0x2f104800
	s_addc_u32 s13, s17, 0
	s_lshl_b64 s[16:17], s[30:31], 2
	s_add_u32 s20, s20, s16
	s_addc_u32 s21, s21, s17
	s_add_u32 s18, s18, s16
	v_and_b32_e32 v33, 15, v36
	s_addc_u32 s19, s19, s17
	v_lshlrev_b32_e32 v144, 2, v33
	v_lshl_add_u64 v[130:131], v[36:37], 2, s[28:29]
	v_cmp_eq_u32_e64 s[38:39], 0, v36
	v_lshlrev_b32_e32 v236, 3, v36
	v_and_b32_e32 v39, -16, v36
	v_lshlrev_b32_e32 v34, 4, v36
	v_lshrrev_b32_e32 v41, 4, v36
	v_lshl_add_u64 v[36:37], s[18:19], 0, v[144:145]
	s_movk_i32 s18, 0xffe0
	s_mov_b32 s19, -1
	v_and_b32_e32 v40, 0xffffff00, v34
	v_lshl_add_u64 v[34:35], s[20:21], 0, v[144:145]
	v_lshl_add_u64 v[36:37], v[36:37], 0, s[18:19]
	v_cmp_gt_u32_e32 vcc, 8, v33
	v_mul_u32_u24_e32 v38, 0x810, v33
	v_readlane_b32 s28, v254, 55
	v_cndmask_b32_e32 v139, v37, v35, vcc
	v_cndmask_b32_e32 v138, v36, v34, vcc
	v_lshl_add_u64 v[34:35], s[6:7], 0, v[144:145]
	s_mov_b64 s[6:7], 0x2c498800
	v_lshl_add_u64 v[140:141], v[34:35], 0, s[6:7]
	s_mul_i32 s6, s56, 0x1020
	v_readlane_b32 s7, v254, 54
	v_ashrrev_i32_e32 v33, 5, v32
	s_add_i32 s17, s7, s6
	s_add_i32 s18, s28, s6
	s_addk_i32 s6, 0x810
	v_add_u32_e32 v33, s58, v33
	v_readlane_b32 s21, v254, 53
	s_add_i32 s19, s7, s6
	v_add_u32_e32 v35, s7, v236
	s_lshl_b32 s7, s56, 8
	v_mul_lo_u32 v33, s59, v33
	v_add3_u32 v34, s21, v40, v144
	s_add_i32 s20, s28, s6
	v_add_u32_e32 v36, s28, v236
	v_add3_u32 v37, v38, v39, s7
	s_lshl_b32 s7, s56, 10
	v_and_or_b32 v237, v41, 1, v33
	v_lshl_add_u32 v238, v32, 2, s21
	v_lshl_add_u64 v[32:33], s[2:3], 0, v[128:129]
	s_mov_b64 s[2:3], 0x23498800
	v_mov_b32_e32 v144, v145
	v_add_u32_e32 v132, 0x100, v128
	v_add_u32_e32 v134, 0x200, v128
	v_add_u32_e32 v136, 0x300, v128
	s_cmp_lt_i32 s56, 4
	v_lshl_add_u64 v[150:151], v[32:33], 0, s[2:3]
	v_mov_b32_e32 v146, v145
	v_mov_b32_e32 v147, v145
	v_add_u32_e32 v239, s6, v35
	v_add_u32_e32 v240, s6, v36
	v_add_u32_e32 v241, 0, v37
	v_add_u32_e32 v242, s7, v34
	v_mov_b64_e32 v[76:77], v[144:145]
	v_mov_b64_e32 v[64:65], v[144:145]
	v_mov_b64_e32 v[68:69], v[144:145]
	v_mov_b64_e32 v[72:73], v[144:145]
	v_mov_b64_e32 v[60:61], v[144:145]
	v_mov_b64_e32 v[56:57], v[144:145]
	v_mov_b64_e32 v[52:53], v[144:145]
	v_mov_b64_e32 v[48:49], v[144:145]
	v_mov_b64_e32 v[32:33], v[144:145]
	v_mov_b64_e32 v[36:37], v[144:145]
	v_mov_b64_e32 v[40:41], v[144:145]
	v_mov_b64_e32 v[44:45], v[144:145]
	s_mov_b32 s34, -1
	v_ashrrev_i32_e32 v133, 31, v132
	v_ashrrev_i32_e32 v135, 31, v134
	v_ashrrev_i32_e32 v137, 31, v136
	s_mov_b32 s16, 0
	v_lshl_add_u64 v[142:143], v[128:129], 2, s[36:37]
	s_cselect_b64 s[56:57], -1, 0
	v_lshl_add_u64 v[148:149], v[128:129], 1, s[4:5]
	v_mov_b64_e32 v[78:79], v[146:147]
	v_mov_b64_e32 v[66:67], v[146:147]
	v_mov_b64_e32 v[70:71], v[146:147]
	v_mov_b64_e32 v[74:75], v[146:147]
	v_mov_b64_e32 v[62:63], v[146:147]
	v_mov_b64_e32 v[58:59], v[146:147]
	v_mov_b64_e32 v[54:55], v[146:147]
	v_mov_b64_e32 v[50:51], v[146:147]
	v_mov_b64_e32 v[34:35], v[146:147]
	v_mov_b64_e32 v[38:39], v[146:147]
	v_mov_b64_e32 v[42:43], v[146:147]
	v_mov_b64_e32 v[46:47], v[146:147]
	global_load_dword v252, v[138:139], off
	s_mov_b32 s97, 0
	s_branch .LBB0_143

; #define LAS __attribute__((address_space(3)))
; __device__ __forceinline__ void lds_barrier() { asm volatile("s_waitcnt lgkmcnt(0)" ::: "memory"); __builtin_amdgcn_s_barrier(); asm volatile("" ::: "memory"); }
; __device__ __forceinline__ float softplus_f(float x) { const float e = __expf(-fabsf(x)), u = 1.f + e; const float l = (u == 1.f) ? e : __logf(u) * (e * __builtin_amdgcn_rcpf(u - 1.f)); return fmaxf(x, 0.f) + l; }
; __device__ __forceinline__ void thin_mfma_partial(LAS unsigned char* L, int wave, int lane) {
;     const int fr = lane & 15, fq = lane >> 4;
;     f32x4 acc = {0.f, 0.f, 0.f, 0.f};
; #pragma unroll
;     for (int s = 0; s < 4; ++s) { const int off = fr * TH_STR + (32 * (4 * wave + s) + 8 * fq) * 2;
;         const bf16x8 ahi = *(LAS const bf16x8*)(L + TH_HHI + off), alo = *(LAS const bf16x8*)(L + TH_HLO + off);
;         const bf16x8 bhi = *(LAS const bf16x8*)(L + TH_THI + off), blo = *(LAS const bf16x8*)(L + TH_TLO + off);
;         acc = __builtin_amdgcn_mfma_f32_16x16x32_bf16(ahi, bhi, acc, 0, 0, 0);
;         acc = __builtin_amdgcn_mfma_f32_16x16x32_bf16(ahi, blo, acc, 0, 0, 0);
;         acc = __builtin_amdgcn_mfma_f32_16x16x32_bf16(alo, bhi, acc, 0, 0, 0); }
;     LAS float* P = (LAS float*)(L + TH_PART) + wave * 256;
; #pragma unroll
;     for (int t2 = 0; t2 < 4; ++t2) P[(4 * fq + t2) * 16 + fr] = acc[t2];
; }
; __device__ __forceinline__ void p1_norm1(const Frame& F, int layer, int probe_rerun) {
;     ...
;         thin_mfma_partial(F.lds, F.wave, lane);
;         lds_barrier();
;         if (F.wave < 4) { const int t16 = F.wave * 64 + lane, srow = t16 >> 4, c = t16 & 15; const float tot = thin_total(F.lds, t16);
;             const float bias = (c < 8) ? dtbf[c] : dtbb[c - 8]; const int grow = (F.blk * NWAVES + (srow >> 1)) * RW + 2 * pi + (srow & 1);
;             if (grow < nrows) DTp[(size_t)grow * 16 + c] = softplus_f(tot + bias); }
.Lp1pf_skip:
	s_waitcnt lgkmcnt(0)
	s_barrier
	v_add_u32_e32 v108, 0x10200, v241
	ds_read_b128 v[80:83], v108
	ds_read_b128 v[84:87], v241
	ds_read_b128 v[88:91], v108 offset:64
	ds_read_b128 v[92:95], v241 offset:64
	ds_read_b128 v[100:103], v241 offset:33024
	ds_read_b128 v[104:107], v241 offset:33088
	s_waitcnt lgkmcnt(4)
	v_mfma_f32_16x16x32_bf16 v[96:99], v[80:83], v[84:87], 0
	v_add_u32_e32 v109, 0x18300, v241
	s_mov_b32 s2, 0x9000
	s_waitcnt lgkmcnt(1)
	v_mfma_f32_16x16x32_bf16 v[80:83], v[80:83], v[100:103], v[96:99]
	s_nop 3
	ds_read_b128 v[96:99], v109
	ds_read_b128 v[100:103], v109 offset:64
	s_waitcnt lgkmcnt(1)
	v_mfma_f32_16x16x32_bf16 v[80:83], v[96:99], v[84:87], v[80:83]
	ds_read_b128 v[84:87], v108 offset:128
	v_mfma_f32_16x16x32_bf16 v[80:83], v[88:91], v[92:95], v[80:83]
	v_mfma_f32_16x16x32_bf16 v[80:83], v[88:91], v[104:107], v[80:83]
	s_waitcnt lgkmcnt(1)
	v_mfma_f32_16x16x32_bf16 v[80:83], v[100:103], v[92:95], v[80:83]
	ds_read_b128 v[88:91], v241 offset:128
	ds_read_b128 v[92:95], v108 offset:192
	ds_read_b128 v[96:99], v241 offset:192
	ds_read_b128 v[100:103], v241 offset:33152
	ds_read_b128 v[104:107], v241 offset:33216
	s_waitcnt lgkmcnt(4)
	v_mfma_f32_16x16x32_bf16 v[80:83], v[84:87], v[88:91], v[80:83]
	s_waitcnt lgkmcnt(1)
	v_mfma_f32_16x16x32_bf16 v[80:83], v[84:87], v[100:103], v[80:83]
	ds_read_b128 v[84:87], v109 offset:128
	ds_read_b128 v[100:103], v109 offset:192
	s_waitcnt lgkmcnt(1)
	v_mfma_f32_16x16x32_bf16 v[80:83], v[84:87], v[88:91], v[80:83]
	v_mfma_f32_16x16x32_bf16 v[80:83], v[92:95], v[96:99], v[80:83]
	v_mfma_f32_16x16x32_bf16 v[80:83], v[92:95], v[104:107], v[80:83]
	s_waitcnt lgkmcnt(0)
	v_mfma_f32_16x16x32_bf16 v[80:83], v[100:103], v[96:99], v[80:83]
	s_nop 7
	ds_write2_b32 v242, v80, v81 offset1:16
	ds_write2_b32 v242, v82, v83 offset0:32 offset1:48
	s_waitcnt lgkmcnt(0)
	s_barrier
	v_add_u32_e32 v80, s21, v237
	v_cmp_gt_i32_e32 vcc, s2, v80
	s_and_b64 s[4:5], s[56:57], vcc
	s_and_saveexec_b64 s[2:3], s[4:5]
	s_cbranch_execz .LBB0_142
	ds_read2st64_b32 v[82:83], v238 offset1:4
	ds_read2st64_b32 v[84:85], v238 offset0:8 offset1:12
	ds_read2st64_b32 v[86:87], v238 offset0:16 offset1:20
	ds_read2st64_b32 v[88:89], v238 offset0:24 offset1:28
	s_mov_b32 s4, 0xbfb8aa3b
	s_waitcnt lgkmcnt(3)
	v_add_f32_e32 v82, 0, v82
	v_add_f32_e32 v82, v82, v83
	s_waitcnt lgkmcnt(2)
	v_add_f32_e32 v82, v82, v84
	v_add_f32_e32 v82, v82, v85
	s_waitcnt lgkmcnt(1)
	v_add_f32_e32 v82, v82, v86
	v_add_f32_e32 v82, v82, v87
	s_waitcnt lgkmcnt(0)
	v_add_f32_e32 v82, v82, v88
	v_add_f32_e32 v82, v82, v89
	v_mov_b32_e32 v87, 0x41b17218
	v_add_f32_e32 v82, v82, v252
	v_mul_f32_e64 v81, |v82|, s4
	v_exp_f32_e32 v83, v81
	s_mov_b32 s4, 0x3f317217
	v_ashrrev_i32_e32 v81, 31, v80
	v_lshlrev_b64 v[80:81], 6, v[80:81]
	v_add_f32_e32 v84, 1.0, v83
	v_cmp_gt_f32_e32 vcc, s22, v84
	v_add_f32_e32 v86, -1.0, v84
	v_rcp_f32_e32 v86, v86
	v_cndmask_b32_e64 v85, 0, 32, vcc
	v_ldexp_f32 v85, v84, v85
	v_log_f32_e32 v85, v85
	v_cndmask_b32_e32 v87, 0, v87, vcc
	v_mul_f32_e32 v86, v83, v86
	v_max_f32_e32 v82, 0, v82
	v_mul_f32_e32 v88, 0x3f317217, v85
	v_fma_f32 v88, v85, s4, -v88
	v_fmac_f32_e32 v88, 0x3377d1cf, v85
	s_mov_b32 s4, 0x7f800000
	v_fmac_f32_e32 v88, 0x3f317217, v85
	v_cmp_lt_f32_e64 vcc, |v85|, s4
	v_lshl_add_u64 v[80:81], v[140:141], 0, v[80:81]
	s_nop 0
	v_cndmask_b32_e32 v85, v85, v88, vcc
	v_sub_f32_e32 v85, v85, v87
	v_mul_f32_e32 v85, v85, v86
	v_cmp_eq_f32_e32 vcc, 1.0, v84
	s_nop 1
	v_cndmask_b32_e32 v83, v85, v83, vcc
	v_add_f32_e32 v82, v82, v83
	global_store_dword v[80:81], v82, off
	s_branch .LBB0_142
